# attention: next sub-tile's Q fetched by LDS-DMA during the current sub-tile (ds_read at the top instead of a waited global load); dense GEMM accumulator zeroing with v_mov_b64
# speedup vs baseline: 1.0036x; 1.0036x over previous
.LBB0_142:
	s_ashr_i32 s9, s8, 31
	s_lshl_b64 s[10:11], s[8:9], 20
	s_add_u32 s10, s33, s10
	s_addc_u32 s11, s44, s11
	s_and_b64 s[38:39], s[2:3], exec
	s_cselect_b32 s9, s11, s15
	s_cselect_b32 s13, s10, s14
	s_add_i32 s38, s58, 0x80
	v_add_u32_e32 v4, s58, v1
	s_add_u32 s60, s14, 0x10000
	v_add_u32_e32 v5, s38, v1
	v_add_u32_e32 v6, s58, v240
	v_add_u32_e32 v7, s38, v240
	v_lshl_add_u32 v245, v4, 12, v239
	s_addc_u32 s61, s15, 0
	v_mov_b32_e32 v4, 0
	v_readlane_b32 s14, v251, 57
	v_lshl_add_u32 v220, v5, 12, v239
	v_lshl_add_u32 v246, v6, 12, v241
	v_lshl_add_u32 v222, v7, 12, v241
	v_mov_b32_e32 v221, v3
	v_mov_b32_e32 v223, v3
	s_mov_b32 s62, -2
	v_readlane_b32 s15, v251, 58
	v_mov_b64_e32 v[4:5], 0
	v_mov_b64_e32 v[6:7], 0
	v_mov_b64_e32 v[8:9], 0
	v_mov_b64_e32 v[10:11], 0
	v_mov_b64_e32 v[12:13], 0
	v_mov_b64_e32 v[14:15], 0
	v_mov_b64_e32 v[16:17], 0
	v_mov_b64_e32 v[18:19], 0
	v_mov_b64_e32 v[20:21], 0
	v_mov_b64_e32 v[22:23], 0
	v_mov_b64_e32 v[24:25], 0
	v_mov_b64_e32 v[26:27], 0
	v_mov_b64_e32 v[28:29], 0
	v_mov_b64_e32 v[30:31], 0
	v_mov_b64_e32 v[32:33], 0
	v_mov_b64_e32 v[34:35], 0
	v_mov_b64_e32 v[36:37], 0
	v_mov_b64_e32 v[38:39], 0
	v_mov_b64_e32 v[40:41], 0
	v_mov_b64_e32 v[42:43], 0
	v_mov_b64_e32 v[44:45], 0
	v_mov_b64_e32 v[46:47], 0
	v_mov_b64_e32 v[48:49], 0
	v_mov_b64_e32 v[50:51], 0
	v_mov_b64_e32 v[52:53], 0
	v_mov_b64_e32 v[54:55], 0
	v_mov_b64_e32 v[56:57], 0
	v_mov_b64_e32 v[58:59], 0
	v_mov_b64_e32 v[60:61], 0
	v_mov_b64_e32 v[62:63], 0
	v_mov_b64_e32 v[64:65], 0
	v_mov_b64_e32 v[66:67], 0
	v_mov_b64_e32 v[68:69], 0
	v_mov_b64_e32 v[70:71], 0
	v_mov_b64_e32 v[72:73], 0
	v_mov_b64_e32 v[74:75], 0
	v_mov_b64_e32 v[76:77], 0
	v_mov_b64_e32 v[78:79], 0
	v_mov_b64_e32 v[80:81], 0
	v_mov_b64_e32 v[82:83], 0
	v_mov_b64_e32 v[88:89], 0
	v_mov_b64_e32 v[90:91], 0
	v_mov_b64_e32 v[92:93], 0
	v_mov_b64_e32 v[94:95], 0
	v_mov_b64_e32 v[96:97], 0
	v_mov_b64_e32 v[98:99], 0
	v_mov_b64_e32 v[100:101], 0
	v_mov_b64_e32 v[102:103], 0
	v_mov_b64_e32 v[104:105], 0
	v_mov_b64_e32 v[106:107], 0
	v_mov_b64_e32 v[108:109], 0
	v_mov_b64_e32 v[110:111], 0
	v_mov_b64_e32 v[112:113], 0
	v_mov_b64_e32 v[114:115], 0
	v_mov_b64_e32 v[116:117], 0
	v_mov_b64_e32 v[118:119], 0
	v_mov_b64_e32 v[120:121], 0
	v_mov_b64_e32 v[122:123], 0
	v_mov_b64_e32 v[124:125], 0
	v_mov_b64_e32 v[126:127], 0
	v_mov_b64_e32 v[128:129], 0
	v_mov_b64_e32 v[130:131], 0
	v_mov_b64_e32 v[132:133], 0
	v_mov_b64_e32 v[134:135], 0
	s_branch .LBB0_145

.LBB0_223:
	s_or_b64 exec, exec, s[2:3]
	s_and_b32 s3, s42, 0xfffff800
	s_add_i32 s2, s10, s26
	v_or_b32_e32 v4, s3, v180
	s_and_b32 s3, s47, 15
	v_lshl_or_b32 v92, s3, 7, v4
	s_ashr_i32 s3, s2, 31
	s_lshl_b64 s[4:5], s[2:3], 2
	v_readlane_b32 s3, v250, 8
	s_add_u32 s4, s3, s4
	v_readlane_b32 s3, v250, 10
	s_waitcnt lgkmcnt(0)
	s_barrier
	s_addc_u32 s5, s3, s5
	global_load_dword v4, v3, s[4:5]
	ds_read2_b32 v[98:99], v182 offset0:159 offset1:160
	ds_read2_b32 v[100:101], v182 offset0:157 offset1:158
	ds_read2_b32 v[102:103], v182 offset0:151 offset1:152
	ds_read2_b32 v[104:105], v182 offset0:149 offset1:150
	ds_read2_b32 v[106:107], v182 offset0:143 offset1:144
	ds_read2_b32 v[108:109], v182 offset0:141 offset1:142
	ds_read2_b32 v[110:111], v182 offset0:135 offset1:136
	ds_read2_b32 v[112:113], v182 offset0:133 offset1:134
	ds_read2_b32 v[114:115], v182 offset0:127 offset1:128
	ds_read2_b32 v[116:117], v182 offset0:125 offset1:126
	ds_read2_b32 v[118:119], v182 offset0:119 offset1:120
	ds_read2_b32 v[120:121], v182 offset0:117 offset1:118
	ds_read2_b32 v[122:123], v182 offset0:111 offset1:112
	ds_read2_b32 v[124:125], v182 offset0:109 offset1:110
	ds_read2_b32 v[126:127], v182 offset0:103 offset1:104
	ds_read2_b32 v[128:129], v182 offset0:101 offset1:102
	ds_read2_b32 v[130:131], v182 offset0:95 offset1:96
	ds_read2_b32 v[132:133], v182 offset0:93 offset1:94
	ds_read2_b32 v[134:135], v182 offset0:87 offset1:88
	ds_read2_b32 v[136:137], v182 offset0:85 offset1:86
	ds_read2_b32 v[138:139], v182 offset0:79 offset1:80
	ds_read2_b32 v[140:141], v182 offset0:77 offset1:78
	ds_read2_b32 v[142:143], v182 offset0:71 offset1:72
	ds_read2_b32 v[144:145], v182 offset0:69 offset1:70
	ds_read2_b32 v[146:147], v182 offset0:63 offset1:64
	ds_read2_b32 v[148:149], v182 offset0:61 offset1:62
	ds_read2_b32 v[150:151], v182 offset0:55 offset1:56
	ds_read2_b32 v[152:153], v182 offset0:53 offset1:54
	ds_read2_b32 v[154:155], v182 offset0:47 offset1:48
	ds_read2_b32 v[156:157], v182 offset0:45 offset1:46
	ds_read2_b32 v[158:159], v182 offset0:39 offset1:40
	ds_read2_b32 v[160:161], v182 offset0:37 offset1:38
	ds_read2_b32 v[162:163], v182 offset0:31 offset1:32
	ds_read2_b32 v[164:165], v182 offset0:29 offset1:30
	ds_read2_b32 v[166:167], v182 offset0:23 offset1:24
	ds_read2_b32 v[168:169], v182 offset0:21 offset1:22
	ds_read2_b32 v[170:171], v182 offset0:15 offset1:16
	ds_read2_b32 v[172:173], v182 offset0:13 offset1:14
	ds_read2_b32 v[174:175], v182 offset0:7 offset1:8
	ds_read2_b32 v[176:177], v182 offset0:5 offset1:6
	v_and_b32_e32 v5, 64, v229
	s_lshl_b32 s2, s2, 6
	v_add_u32_e32 v5, 64, v5
	s_ashr_i32 s3, s2, 31
	s_lshl_b64 s[2:3], s[2:3], 1
	v_lshl_add_u64 v[94:95], v[88:89], 0, s[2:3]
	s_mov_b32 s45, 0
	v_lshl_add_u64 v[96:97], v[90:91], 0, s[2:3]
	s_and_b64 s[80:81], s[50:51], s[40:41]
	s_and_b64 s[82:83], s[52:53], s[40:41]
	s_and_b64 s[84:85], s[54:55], s[40:41]
	s_and_b64 s[86:87], s[56:57], s[40:41]
	s_and_b64 s[88:89], s[58:59], s[40:41]
	s_and_b64 s[90:91], s[60:61], s[40:41]
	s_and_b64 s[92:93], s[62:63], s[40:41]
	s_and_b64 s[94:95], s[64:65], s[40:41]
	s_and_b64 s[96:97], s[66:67], s[40:41]
	s_and_b64 s[2:3], s[68:69], s[40:41]
	s_and_b64 s[4:5], s[70:71], s[40:41]
	s_and_b64 s[6:7], s[72:73], s[40:41]
	s_and_b64 s[8:9], s[74:75], s[40:41]
	s_and_b64 s[10:11], s[76:77], s[40:41]
	s_and_b64 s[12:13], s[78:79], s[40:41]
	s_and_b64 s[14:15], s[48:49], s[40:41]
	s_mov_b32 s39, 0
	s_waitcnt vmcnt(0)
	v_mul_f32_e32 v193, 0x3fb8aa3b, v4
	v_xor_b32_e32 v4, 32, v229
	v_cmp_lt_i32_e32 vcc, v4, v5
	s_nop 1
	v_cndmask_b32_e32 v4, v229, v4, vcc
	v_lshlrev_b32_e32 v194, 2, v4
	v_lshrrev_b32_e32 v255, 6, v0
	s_nop 0
	v_readfirstlane_b32 s100, v255
	s_lshl_b32 s100, s100, 12
	s_add_u32 s100, s100, 0x14000
	v_lshl_add_u32 v255, v229, 4, s100
	v_ashrrev_i32_e32 v85, 31, v92
	v_mov_b32_e32 v84, v92
	v_lshlrev_b64 v[84:85], 12, v[84:85]
	v_lshl_add_u64 v[84:85], v[94:95], 0, v[84:85]
	v_lshl_add_u64 v[86:87], v[84:85], 0, 32
	v_lshl_add_u64 v[242:243], v[84:85], 0, 64
	v_lshl_add_u64 v[244:245], v[242:243], 0, 32
	s_mov_b32 m0, s100
	s_nop 0
	global_load_lds_dwordx4 v[84:85], off
	s_bitset1_b32 m0, 10
	s_nop 0
	global_load_lds_dwordx4 v[86:87], off
	s_bitset0_b32 m0, 10
	s_bitset1_b32 m0, 11
	s_nop 0
	global_load_lds_dwordx4 v[242:243], off
	s_bitset1_b32 m0, 10
	s_nop 0
	global_load_lds_dwordx4 v[244:245], off
	s_waitcnt vmcnt(0)
.LBB0_224:
	v_ashrrev_i32_e32 v93, 31, v92
	v_lshlrev_b64 v[178:179], 12, v[92:93]
	v_lshl_add_u64 v[8:9], v[94:95], 0, v[178:179]
	s_waitcnt vmcnt(8)
	ds_read_b128 v[4:7], v255
	ds_read_b128 v[196:199], v255 offset:1024
	ds_read_b128 v[208:211], v255 offset:2048
	ds_read_b128 v[212:215], v255 offset:3072
	v_add_u32_e32 v93, s45, v188
	ds_read_b128 v[8:11], v93
	ds_read_b128 v[12:15], v93 offset:32
	s_mov_b32 s33, 0xf149f2ca
	s_add_i32 s38, s39, 1
	s_cmp_gt_u32 s39, 2
	s_cselect_b64 vcc, -1, 0
	s_or_b64 vcc, s[40:41], vcc
	s_cmp_gt_u32 s39, 1
	v_add_u32_e32 v92, 32, v92
	s_waitcnt lgkmcnt(0)
	v_mfma_f32_32x32x16_bf16 v[68:83], v[8:11], v[4:7], 0
	v_ashrrev_i32_e32 v85, 31, v92
	v_mov_b32_e32 v84, v92
	v_lshlrev_b64 v[84:85], 12, v[84:85]
	v_lshl_add_u64 v[84:85], v[94:95], 0, v[84:85]
	v_lshl_add_u64 v[86:87], v[84:85], 0, 32
	v_lshl_add_u64 v[242:243], v[84:85], 0, 64
	v_lshl_add_u64 v[244:245], v[242:243], 0, 32
	s_mov_b32 m0, s100
	s_nop 0
	global_load_lds_dwordx4 v[84:85], off
	s_bitset1_b32 m0, 10
	s_nop 0
	global_load_lds_dwordx4 v[86:87], off
	s_bitset0_b32 m0, 10
	s_bitset1_b32 m0, 11
	s_nop 0
	global_load_lds_dwordx4 v[242:243], off
	s_bitset1_b32 m0, 10
	s_nop 0
	global_load_lds_dwordx4 v[244:245], off
	ds_read_b128 v[8:11], v93 offset:64
	ds_read_b128 v[216:219], v93 offset:18464
	v_mfma_f32_32x32x16_bf16 v[68:83], v[12:15], v[196:199], v[68:83]
	s_waitcnt lgkmcnt(1)
	v_mfma_f32_32x32x16_bf16 v[68:83], v[8:11], v[208:211], v[68:83]
	ds_read_b128 v[8:11], v93 offset:96
	s_waitcnt lgkmcnt(0)
	v_mfma_f32_32x32x16_bf16 v[68:83], v[8:11], v[212:215], v[68:83]
	ds_read_b128 v[8:11], v93 offset:4608
	s_waitcnt lgkmcnt(0)
	v_mfma_f32_32x32x16_bf16 v[52:67], v[8:11], v[4:7], 0
	ds_read_b128 v[8:11], v93 offset:4640
	s_nop 7
	v_add_f32_e32 v68, v68, v99
	v_add_f32_e32 v69, v69, v98
	v_cndmask_b32_e64 v68, v234, v68, s[80:81]
	v_cndmask_b32_e64 v69, v234, v69, s[82:83]
	v_add_f32_e32 v70, v70, v101
	v_add_f32_e32 v71, v71, v100
	s_waitcnt lgkmcnt(0)
	v_mfma_f32_32x32x16_bf16 v[52:67], v[8:11], v[196:199], v[52:67]
	ds_read_b128 v[8:11], v93 offset:4672
	v_cndmask_b32_e64 v70, v234, v70, s[84:85]
	v_cndmask_b32_e64 v71, v234, v71, s[86:87]
	v_add_f32_e32 v72, v72, v103
	v_add_f32_e32 v73, v73, v102
	v_cndmask_b32_e64 v72, v234, v72, s[88:89]
	v_cndmask_b32_e64 v73, v234, v73, s[90:91]
	s_waitcnt lgkmcnt(0)
	v_mfma_f32_32x32x16_bf16 v[52:67], v[8:11], v[208:211], v[52:67]
	ds_read_b128 v[8:11], v93 offset:4704
	v_add_f32_e32 v74, v74, v105
	v_add_f32_e32 v75, v75, v104
	v_cndmask_b32_e64 v74, v234, v74, s[92:93]
	v_cndmask_b32_e64 v75, v234, v75, s[94:95]
	v_add_f32_e32 v76, v76, v107
	v_add_f32_e32 v77, v77, v106
	s_waitcnt lgkmcnt(0)
	v_mfma_f32_32x32x16_bf16 v[52:67], v[8:11], v[212:215], v[52:67]
	ds_read_b128 v[8:11], v93 offset:9216
	v_cndmask_b32_e64 v76, v234, v76, s[96:97]
	v_cndmask_b32_e64 v77, v234, v77, s[2:3]
	v_add_f32_e32 v78, v78, v109
	v_add_f32_e32 v79, v79, v108
	v_cndmask_b32_e64 v78, v234, v78, s[4:5]
	v_cndmask_b32_e64 v79, v234, v79, s[6:7]
	s_waitcnt lgkmcnt(0)
	v_mfma_f32_32x32x16_bf16 v[36:51], v[8:11], v[4:7], 0
	ds_read_b128 v[8:11], v93 offset:9248
	v_add_f32_e32 v80, v80, v111
	v_add_f32_e32 v81, v81, v110
	v_cndmask_b32_e64 v80, v234, v80, s[8:9]
	v_cndmask_b32_e64 v81, v234, v81, s[10:11]
	v_add_f32_e32 v82, v82, v113
	v_add_f32_e32 v83, v83, v112
	s_waitcnt lgkmcnt(0)
	v_mfma_f32_32x32x16_bf16 v[36:51], v[8:11], v[196:199], v[36:51]
	ds_read_b128 v[8:11], v93 offset:9280
	v_cndmask_b32_e64 v82, v234, v82, s[12:13]
	v_cndmask_b32_e64 v83, v234, v83, s[14:15]
	v_add_f32_e32 v52, v52, v115
	v_add_f32_e32 v53, v53, v114
	v_cndmask_b32_e32 v52, v234, v52, vcc
	v_cndmask_b32_e32 v53, v234, v53, vcc
	s_waitcnt lgkmcnt(0)
	v_mfma_f32_32x32x16_bf16 v[36:51], v[8:11], v[208:211], v[36:51]
	ds_read_b128 v[8:11], v93 offset:9312
	v_add_f32_e32 v54, v54, v117
	v_add_f32_e32 v55, v55, v116
	v_cndmask_b32_e32 v54, v234, v54, vcc
	v_cndmask_b32_e32 v55, v234, v55, vcc
	v_add_f32_e32 v56, v56, v119
	v_add_f32_e32 v57, v57, v118
	s_waitcnt lgkmcnt(0)
	v_mfma_f32_32x32x16_bf16 v[36:51], v[8:11], v[212:215], v[36:51]
	ds_read_b128 v[8:11], v93 offset:13824
	v_cndmask_b32_e32 v56, v234, v56, vcc
	v_cndmask_b32_e32 v57, v234, v57, vcc
	v_add_f32_e32 v58, v58, v121
	v_add_f32_e32 v59, v59, v120
	v_cndmask_b32_e32 v58, v234, v58, vcc
	v_cndmask_b32_e32 v59, v234, v59, vcc
	s_waitcnt lgkmcnt(0)
	v_mfma_f32_32x32x16_bf16 v[20:35], v[8:11], v[4:7], 0
	ds_read_b128 v[8:11], v93 offset:13856
	v_add_f32_e32 v60, v60, v123
	v_add_f32_e32 v61, v61, v122
	v_cndmask_b32_e32 v60, v234, v60, vcc
	v_cndmask_b32_e32 v61, v234, v61, vcc
	v_add_f32_e32 v62, v62, v125
	v_add_f32_e32 v63, v63, v124
	s_waitcnt lgkmcnt(0)
	v_mfma_f32_32x32x16_bf16 v[20:35], v[8:11], v[196:199], v[20:35]
	ds_read_b128 v[8:11], v93 offset:13888
	v_cndmask_b32_e32 v62, v234, v62, vcc
	v_cndmask_b32_e32 v63, v234, v63, vcc
	v_add_f32_e32 v64, v64, v127
	v_add_f32_e32 v65, v65, v126
	v_add_f32_e32 v66, v66, v129
	v_add_f32_e32 v67, v67, v128
	s_waitcnt lgkmcnt(0)
	v_mfma_f32_32x32x16_bf16 v[20:35], v[8:11], v[208:211], v[20:35]
	ds_read_b128 v[8:11], v93 offset:13920
	v_cndmask_b32_e32 v64, v234, v64, vcc
	v_cndmask_b32_e32 v65, v234, v65, vcc
	v_cndmask_b32_e32 v66, v234, v66, vcc
	v_cndmask_b32_e32 v67, v234, v67, vcc
	s_cselect_b64 vcc, -1, 0
	s_or_b64 vcc, s[40:41], vcc
	s_waitcnt lgkmcnt(0)
	v_mfma_f32_32x32x16_bf16 v[20:35], v[8:11], v[212:215], v[20:35]
	ds_read_b128 v[8:11], v93 offset:18432
	v_add_f32_e32 v36, v36, v131
	v_add_f32_e32 v37, v37, v130
	v_cndmask_b32_e32 v36, v234, v36, vcc
	v_cndmask_b32_e32 v37, v234, v37, vcc
	v_add_f32_e32 v38, v38, v133
	v_add_f32_e32 v39, v39, v132
	s_waitcnt lgkmcnt(0)
	v_mfma_f32_32x32x16_bf16 v[4:19], v[8:11], v[4:7], 0
	v_cndmask_b32_e32 v38, v234, v38, vcc
	v_cndmask_b32_e32 v39, v234, v39, vcc
	v_add_f32_e32 v40, v40, v135
	v_add_f32_e32 v41, v41, v134
	v_cndmask_b32_e32 v40, v234, v40, vcc
	v_cndmask_b32_e32 v41, v234, v41, vcc
	v_add_f32_e32 v42, v42, v137
	v_mfma_f32_32x32x16_bf16 v[4:19], v[216:219], v[196:199], v[4:19]
	ds_read_b128 v[196:199], v93 offset:18496
	v_add_f32_e32 v43, v43, v136
	v_cndmask_b32_e32 v42, v234, v42, vcc
	v_cndmask_b32_e32 v43, v234, v43, vcc
	v_add_f32_e32 v44, v44, v139
	v_add_f32_e32 v45, v45, v138
	v_cndmask_b32_e32 v44, v234, v44, vcc
	s_waitcnt lgkmcnt(0)
	v_mfma_f32_32x32x16_bf16 v[4:19], v[196:199], v[208:211], v[4:19]
	ds_read_b128 v[196:199], v93 offset:18528
	v_max3_f32 v93, v68, s33, v69
	v_max3_f32 v93, v93, v70, v71
	v_max3_f32 v93, v93, v72, v73
	v_max3_f32 v93, v93, v74, v75
	v_max3_f32 v93, v93, v76, v77
	v_max3_f32 v93, v93, v78, v79
	v_max3_f32 v93, v93, v80, v81
	v_max3_f32 v93, v93, v82, v83
	v_max3_f32 v93, v93, v52, v53
	v_max3_f32 v93, v93, v54, v55
	v_max3_f32 v93, v93, v56, v57
	v_max3_f32 v93, v93, v58, v59
	v_max3_f32 v93, v93, v60, v61
	v_max3_f32 v93, v93, v62, v63
	v_max3_f32 v93, v93, v64, v65
	v_max3_f32 v93, v93, v66, v67
	v_max3_f32 v93, v93, v36, v37
	v_max3_f32 v93, v93, v38, v39
	v_max3_f32 v93, v93, v40, v41
	v_max3_f32 v93, v93, v42, v43
	v_cndmask_b32_e32 v45, v234, v45, vcc
	v_add_f32_e32 v46, v46, v141
	v_add_f32_e32 v47, v47, v140
	v_max3_f32 v93, v93, v44, v45
	v_cndmask_b32_e32 v46, v234, v46, vcc
	v_cndmask_b32_e32 v47, v234, v47, vcc
	v_add_f32_e32 v48, v48, v143
	v_add_f32_e32 v49, v49, v142
	s_or_b32 s33, s39, s44
	v_max3_f32 v93, v93, v46, v47
	v_cndmask_b32_e32 v48, v234, v48, vcc
	v_cndmask_b32_e32 v49, v234, v49, vcc
	v_add_f32_e32 v50, v50, v145
	v_add_f32_e32 v51, v51, v144
	s_cmp_eq_u32 s33, 0
	s_waitcnt lgkmcnt(0)
	v_mfma_f32_32x32x16_bf16 v[4:19], v[196:199], v[212:215], v[4:19]
	v_max3_f32 v93, v93, v48, v49
	v_cndmask_b32_e32 v50, v234, v50, vcc
	v_cndmask_b32_e32 v51, v234, v51, vcc
	s_cselect_b64 vcc, -1, 0
	v_add_f32_e32 v20, v20, v147
	v_add_f32_e32 v21, v21, v146
	v_max3_f32 v93, v93, v50, v51
	v_cndmask_b32_e32 v20, v20, v234, vcc
	v_cndmask_b32_e32 v21, v21, v234, vcc
	v_add_f32_e32 v22, v22, v149
	v_add_f32_e32 v23, v23, v148
	v_max3_f32 v93, v93, v20, v21
	v_cndmask_b32_e32 v22, v22, v234, vcc
	v_cndmask_b32_e32 v23, v23, v234, vcc
	v_add_f32_e32 v24, v24, v151
	v_add_f32_e32 v25, v25, v150
	v_max3_f32 v93, v93, v22, v23
	v_cndmask_b32_e32 v24, v24, v234, vcc
	v_cndmask_b32_e32 v25, v25, v234, vcc
	v_add_f32_e32 v26, v26, v153
	v_add_f32_e32 v27, v27, v152
	v_max3_f32 v93, v93, v24, v25
	v_cndmask_b32_e32 v26, v26, v234, vcc
	v_cndmask_b32_e32 v27, v27, v234, vcc
	v_add_f32_e32 v28, v28, v155
	v_add_f32_e32 v29, v29, v154
	v_max3_f32 v93, v93, v26, v27
	v_cndmask_b32_e32 v28, v28, v234, vcc
	v_cndmask_b32_e32 v29, v29, v234, vcc
	v_add_f32_e32 v30, v30, v157
	v_add_f32_e32 v31, v31, v156
	v_max3_f32 v93, v93, v28, v29
	v_cndmask_b32_e32 v30, v30, v234, vcc
	v_cndmask_b32_e32 v31, v31, v234, vcc
	v_add_f32_e32 v32, v32, v159
	v_add_f32_e32 v33, v33, v158
	v_max3_f32 v93, v93, v30, v31
	v_cndmask_b32_e32 v32, v32, v234, vcc
	v_cndmask_b32_e32 v33, v33, v234, vcc
	v_add_f32_e32 v34, v34, v161
	v_add_f32_e32 v35, v35, v160
	v_max3_f32 v93, v93, v32, v33
	v_cndmask_b32_e32 v34, v34, v234, vcc
	v_cndmask_b32_e32 v35, v35, v234, vcc
	v_add_f32_e32 v4, v4, v163
	v_add_f32_e32 v5, v5, v162
	v_max3_f32 v93, v93, v34, v35
	v_cndmask_b32_e64 v4, v4, v234, s[50:51]
	v_cndmask_b32_e64 v5, v5, v234, s[52:53]
	v_add_f32_e32 v6, v6, v165
	v_add_f32_e32 v7, v7, v164
	v_max3_f32 v93, v93, v4, v5
	v_cndmask_b32_e64 v6, v6, v234, s[54:55]
	v_cndmask_b32_e64 v7, v7, v234, s[56:57]
	v_add_f32_e32 v8, v8, v167
	v_add_f32_e32 v9, v9, v166
	v_max3_f32 v93, v93, v6, v7
	v_cndmask_b32_e64 v8, v8, v234, s[58:59]
	v_cndmask_b32_e64 v9, v9, v234, s[60:61]
	v_add_f32_e32 v10, v10, v169
	v_add_f32_e32 v11, v11, v168
	v_max3_f32 v93, v93, v8, v9
	v_cndmask_b32_e64 v10, v10, v234, s[62:63]
	v_cndmask_b32_e64 v11, v11, v234, s[64:65]
	v_add_f32_e32 v12, v12, v171
	v_add_f32_e32 v13, v13, v170
	v_max3_f32 v93, v93, v10, v11
	v_cndmask_b32_e64 v12, v12, v234, s[66:67]
	v_cndmask_b32_e64 v13, v13, v234, s[68:69]
	v_add_f32_e32 v14, v14, v173
	v_add_f32_e32 v15, v15, v172
	v_max3_f32 v93, v93, v12, v13
	v_cndmask_b32_e64 v14, v14, v234, s[70:71]
	v_cndmask_b32_e64 v15, v15, v234, s[72:73]
	v_add_f32_e32 v16, v16, v175
	v_add_f32_e32 v17, v17, v174
	v_max3_f32 v93, v93, v14, v15
	v_cndmask_b32_e64 v16, v16, v234, s[74:75]
	v_cndmask_b32_e64 v17, v17, v234, s[76:77]
	v_add_f32_e32 v18, v18, v177
	v_add_f32_e32 v19, v19, v176
	v_max3_f32 v93, v93, v16, v17
	v_cndmask_b32_e64 v18, v18, v234, s[78:79]
	v_cndmask_b32_e64 v19, v19, v234, s[48:49]
	v_max3_f32 v93, v93, v18, v19
	ds_bpermute_b32 v195, v194, v93
	s_mov_b32 s39, s38
	s_waitcnt lgkmcnt(0)
	v_max3_f32 v200, v93, v195, v193
	v_sub_f32_e32 v68, v68, v200
	v_exp_f32_e32 v201, v68
	v_sub_f32_e32 v69, v69, v200
	v_exp_f32_e32 v204, v69
	v_sub_f32_e32 v69, v70, v200
	v_exp_f32_e32 v205, v69
	v_sub_f32_e32 v69, v71, v200
	v_exp_f32_e32 v206, v69
	v_sub_f32_e32 v69, v72, v200
	v_add_f32_e32 v68, 0, v201
	v_exp_f32_e32 v207, v69
	v_sub_f32_e32 v69, v73, v200
	v_add_f32_e32 v68, v204, v68
	v_exp_f32_e32 v239, v69
	v_sub_f32_e32 v69, v74, v200
	v_add_f32_e32 v68, v205, v68
	v_exp_f32_e32 v240, v69
	v_sub_f32_e32 v69, v75, v200
	v_add_f32_e32 v68, v206, v68
	v_exp_f32_e32 v241, v69
	v_sub_f32_e32 v69, v76, v200
	v_add_f32_e32 v68, v207, v68
	v_exp_f32_e32 v220, v69
	v_sub_f32_e32 v69, v77, v200
	v_add_f32_e32 v68, v239, v68
	v_exp_f32_e32 v221, v69
	v_sub_f32_e32 v69, v78, v200
	v_add_f32_e32 v68, v240, v68
	v_exp_f32_e32 v222, v69
	v_sub_f32_e32 v69, v79, v200
	v_add_f32_e32 v68, v241, v68
	v_exp_f32_e32 v223, v69
	v_sub_f32_e32 v69, v80, v200
	v_add_f32_e32 v68, v220, v68
	v_exp_f32_e32 v224, v69
	v_sub_f32_e32 v69, v81, v200
	v_add_f32_e32 v68, v221, v68
	v_exp_f32_e32 v225, v69
	v_sub_f32_e32 v69, v82, v200
	v_add_f32_e32 v68, v222, v68
	v_exp_f32_e32 v226, v69
	v_sub_f32_e32 v69, v83, v200
	v_add_f32_e32 v68, v223, v68
	v_exp_f32_e32 v227, v69
	v_sub_f32_e32 v52, v52, v200
	v_add_f32_e32 v68, v224, v68
	v_exp_f32_e32 v212, v52
	v_sub_f32_e32 v53, v53, v200
	v_add_f32_e32 v68, v225, v68
	v_exp_f32_e32 v213, v53
	v_sub_f32_e32 v53, v54, v200
	v_add_f32_e32 v68, v226, v68
	v_exp_f32_e32 v214, v53
	v_sub_f32_e32 v53, v55, v200
	v_add_f32_e32 v68, v227, v68
	v_exp_f32_e32 v215, v53
	v_sub_f32_e32 v53, v56, v200
	v_add_f32_e32 v52, v212, v68
	v_exp_f32_e32 v216, v53
	v_sub_f32_e32 v53, v57, v200
	v_add_f32_e32 v52, v213, v52
	v_exp_f32_e32 v217, v53
	v_sub_f32_e32 v53, v58, v200
	v_add_f32_e32 v52, v214, v52
	v_exp_f32_e32 v218, v53
	v_sub_f32_e32 v53, v59, v200
	v_add_f32_e32 v52, v215, v52
	v_exp_f32_e32 v219, v53
	v_sub_f32_e32 v53, v60, v200
	v_add_f32_e32 v52, v216, v52
	v_exp_f32_e32 v196, v53
	v_sub_f32_e32 v53, v61, v200
	v_add_f32_e32 v52, v217, v52
	v_exp_f32_e32 v197, v53
	v_sub_f32_e32 v53, v62, v200
	v_add_f32_e32 v52, v218, v52
	v_exp_f32_e32 v198, v53
	v_sub_f32_e32 v53, v63, v200
	v_add_f32_e32 v52, v219, v52
	v_exp_f32_e32 v199, v53
	v_sub_f32_e32 v53, v64, v200
	v_add_f32_e32 v52, v196, v52
	v_exp_f32_e32 v208, v53
	v_sub_f32_e32 v53, v65, v200
	v_add_f32_e32 v52, v197, v52
	v_exp_f32_e32 v209, v53
	v_sub_f32_e32 v53, v66, v200
	v_add_f32_e32 v52, v198, v52
	v_exp_f32_e32 v210, v53
	v_sub_f32_e32 v53, v67, v200
	v_add_f32_e32 v52, v199, v52
	v_exp_f32_e32 v211, v53
	v_sub_f32_e32 v36, v36, v200
	v_add_f32_e32 v52, v208, v52
	v_exp_f32_e32 v36, v36
	v_sub_f32_e32 v37, v37, v200
	v_add_f32_e32 v52, v209, v52
	v_exp_f32_e32 v37, v37
	v_sub_f32_e32 v38, v38, v200
	v_add_f32_e32 v52, v210, v52
	v_exp_f32_e32 v38, v38
	v_sub_f32_e32 v39, v39, v200
	v_add_f32_e32 v52, v211, v52
	v_exp_f32_e32 v39, v39
	v_sub_f32_e32 v40, v40, v200
	v_add_f32_e32 v52, v36, v52
	v_exp_f32_e32 v40, v40
	v_sub_f32_e32 v41, v41, v200
	v_add_f32_e32 v52, v37, v52
	v_exp_f32_e32 v41, v41
	v_sub_f32_e32 v42, v42, v200
	v_add_f32_e32 v52, v38, v52
	v_exp_f32_e32 v42, v42
	v_sub_f32_e32 v43, v43, v200
	v_add_f32_e32 v52, v39, v52
	v_exp_f32_e32 v43, v43
	v_sub_f32_e32 v44, v44, v200
	v_add_f32_e32 v52, v40, v52
	v_exp_f32_e32 v78, v44
	v_sub_f32_e32 v45, v45, v200
	v_add_f32_e32 v52, v41, v52
	v_exp_f32_e32 v79, v45
	v_sub_f32_e32 v45, v46, v200
	v_add_f32_e32 v52, v42, v52
	v_exp_f32_e32 v80, v45
	v_sub_f32_e32 v45, v47, v200
	v_add_f32_e32 v52, v43, v52
	v_exp_f32_e32 v81, v45
	v_sub_f32_e32 v45, v48, v200
	v_add_f32_e32 v44, v78, v52
	v_exp_f32_e32 v82, v45
	v_sub_f32_e32 v45, v49, v200
	v_add_f32_e32 v44, v79, v44
	v_exp_f32_e32 v83, v45
	v_sub_f32_e32 v45, v50, v200
	v_add_f32_e32 v44, v80, v44
	v_exp_f32_e32 v93, v45
	v_sub_f32_e32 v45, v51, v200
	v_add_f32_e32 v44, v81, v44
	v_exp_f32_e32 v195, v45
	v_sub_f32_e32 v20, v20, v200
	v_add_f32_e32 v44, v82, v44
	v_exp_f32_e32 v70, v20
	v_sub_f32_e32 v21, v21, v200
	v_add_f32_e32 v44, v83, v44
	v_exp_f32_e32 v71, v21
	v_sub_f32_e32 v21, v22, v200
	v_add_f32_e32 v44, v93, v44
	v_exp_f32_e32 v72, v21
	v_sub_f32_e32 v21, v23, v200
	v_add_f32_e32 v44, v195, v44
	v_exp_f32_e32 v73, v21
	v_sub_f32_e32 v21, v24, v200
	v_add_f32_e32 v20, v70, v44
	v_exp_f32_e32 v74, v21
	v_sub_f32_e32 v21, v25, v200
	v_add_f32_e32 v20, v71, v20
	v_exp_f32_e32 v75, v21
	v_sub_f32_e32 v21, v26, v200
	v_add_f32_e32 v20, v72, v20
	v_exp_f32_e32 v76, v21
	v_sub_f32_e32 v21, v27, v200
	v_add_f32_e32 v20, v73, v20
	v_exp_f32_e32 v77, v21
	v_sub_f32_e32 v21, v28, v200
	v_add_f32_e32 v20, v74, v20
	v_exp_f32_e32 v62, v21
	v_sub_f32_e32 v21, v29, v200
	v_add_f32_e32 v20, v75, v20
	v_exp_f32_e32 v63, v21
	v_sub_f32_e32 v21, v30, v200
	v_add_f32_e32 v20, v76, v20
	v_exp_f32_e32 v64, v21
	v_sub_f32_e32 v21, v31, v200
	v_add_f32_e32 v20, v77, v20
	v_exp_f32_e32 v65, v21
	v_sub_f32_e32 v21, v32, v200
	v_add_f32_e32 v20, v62, v20
	v_exp_f32_e32 v66, v21
	v_sub_f32_e32 v21, v33, v200
	v_add_f32_e32 v20, v63, v20
	v_exp_f32_e32 v67, v21
	v_sub_f32_e32 v21, v34, v200
	v_add_f32_e32 v20, v64, v20
	v_exp_f32_e32 v68, v21
	v_sub_f32_e32 v21, v35, v200
	v_add_f32_e32 v20, v65, v20
	v_exp_f32_e32 v69, v21
	v_sub_f32_e32 v4, v4, v200
	v_add_f32_e32 v20, v66, v20
	v_exp_f32_e32 v54, v4
	v_sub_f32_e32 v5, v5, v200
	v_add_f32_e32 v20, v67, v20
	v_exp_f32_e32 v55, v5
	v_sub_f32_e32 v5, v6, v200
	v_add_f32_e32 v20, v68, v20
	v_exp_f32_e32 v56, v5
	v_sub_f32_e32 v5, v7, v200
	v_add_f32_e32 v20, v69, v20
	v_exp_f32_e32 v57, v5
	v_sub_f32_e32 v5, v8, v200
	v_add_f32_e32 v4, v54, v20
	v_exp_f32_e32 v58, v5
	v_sub_f32_e32 v5, v9, v200
	v_add_f32_e32 v4, v55, v4
	v_exp_f32_e32 v59, v5
	v_sub_f32_e32 v5, v10, v200
	v_add_f32_e32 v4, v56, v4
	v_exp_f32_e32 v60, v5
	v_sub_f32_e32 v5, v11, v200
	v_add_f32_e32 v4, v57, v4
	v_exp_f32_e32 v61, v5
	v_sub_f32_e32 v5, v12, v200
	v_add_f32_e32 v4, v58, v4
	v_exp_f32_e32 v46, v5
	v_sub_f32_e32 v5, v13, v200
	v_add_f32_e32 v4, v59, v4
	v_exp_f32_e32 v47, v5
	v_sub_f32_e32 v5, v14, v200
	v_add_f32_e32 v4, v60, v4
	v_exp_f32_e32 v48, v5
	v_sub_f32_e32 v5, v15, v200
	v_add_f32_e32 v4, v61, v4
	v_exp_f32_e32 v49, v5
	v_sub_f32_e32 v5, v16, v200
	v_add_f32_e32 v4, v46, v4
	v_exp_f32_e32 v50, v5
	v_sub_f32_e32 v5, v17, v200
	v_add_f32_e32 v4, v47, v4
	v_exp_f32_e32 v51, v5
	v_sub_f32_e32 v5, v18, v200
	v_add_f32_e32 v4, v48, v4
	v_exp_f32_e32 v52, v5
	v_sub_f32_e32 v5, v19, v200
	v_add_f32_e32 v4, v49, v4
	v_exp_f32_e32 v53, v5
	v_add_f32_e32 v4, v50, v4
	v_add_f32_e32 v4, v51, v4
	v_add_f32_e32 v4, v52, v4
	v_add_f32_e32 v4, v53, v4
	v_sub_f32_e32 v6, v193, v200
	ds_bpermute_b32 v5, v194, v4
	v_exp_f32_e32 v44, v6
	v_cvt_pk_bf16_f32 v6, v207, v239
	v_add_u32_e32 v239, s45, v187
	ds_read_b64_tr_b16 v[8:9], v239 offset:36864
	ds_read_b64_tr_b16 v[10:11], v239 offset:38016
	s_waitcnt lgkmcnt(2)
	v_add_f32_e32 v45, v4, v5
	v_cvt_pk_bf16_f32 v4, v201, v204
	v_cvt_pk_bf16_f32 v5, v205, v206
	v_cvt_pk_bf16_f32 v7, v240, v241
	v_cvt_pk_bf16_f32 v220, v220, v221
	v_cvt_pk_bf16_f32 v221, v222, v223
	s_waitcnt lgkmcnt(0)
	v_mfma_f32_32x32x16_bf16 v[20:35], v[8:11], v[4:7], 0
	ds_read_b64_tr_b16 v[8:9], v239 offset:36928
	ds_read_b64_tr_b16 v[10:11], v239 offset:38080
	v_cvt_pk_bf16_f32 v222, v224, v225
	v_cvt_pk_bf16_f32 v223, v226, v227
	ds_read_b64_tr_b16 v[224:225], v239 offset:39168
	ds_read_b64_tr_b16 v[226:227], v239 offset:40320
	v_cvt_pk_bf16_f32 v212, v212, v213
	v_cvt_pk_bf16_f32 v213, v214, v215
	v_cvt_pk_bf16_f32 v214, v216, v217
	s_waitcnt lgkmcnt(2)
	v_mfma_f32_32x32x16_bf16 v[4:19], v[8:11], v[4:7], 0
	v_cvt_pk_bf16_f32 v215, v218, v219
	v_cvt_pk_bf16_f32 v196, v196, v197
	v_cvt_pk_bf16_f32 v197, v198, v199
	v_cvt_pk_bf16_f32 v198, v208, v209
	v_cvt_pk_bf16_f32 v199, v210, v211
	v_cvt_pk_bf16_f32 v36, v36, v37
	v_cvt_pk_bf16_f32 v37, v38, v39
	s_waitcnt lgkmcnt(0)
	v_mfma_f32_32x32x16_bf16 v[20:35], v[224:227], v[220:223], v[20:35]
	ds_read_b64_tr_b16 v[224:225], v239 offset:39232
	ds_read_b64_tr_b16 v[226:227], v239 offset:40384
	ds_read_b64_tr_b16 v[216:217], v239 offset:41472
	ds_read_b64_tr_b16 v[218:219], v239 offset:42624
	v_cvt_pk_bf16_f32 v38, v40, v41
	v_cvt_pk_bf16_f32 v39, v42, v43
	s_addk_i32 s45, 0x1200
	s_cmpk_eq_i32 s45, 0x4800
	s_waitcnt lgkmcnt(2)
	v_mfma_f32_32x32x16_bf16 v[4:19], v[224:227], v[220:223], v[4:19]
	s_waitcnt lgkmcnt(0)
	v_mfma_f32_32x32x16_bf16 v[20:35], v[216:219], v[212:215], v[20:35]
	ds_read_b64_tr_b16 v[216:217], v239 offset:41536
	ds_read_b64_tr_b16 v[218:219], v239 offset:42688
	ds_read_b64_tr_b16 v[208:209], v239 offset:43776
	ds_read_b64_tr_b16 v[210:211], v239 offset:44928
	s_waitcnt lgkmcnt(2)
	v_mfma_f32_32x32x16_bf16 v[4:19], v[216:219], v[212:215], v[4:19]
	s_waitcnt lgkmcnt(0)
	v_mfma_f32_32x32x16_bf16 v[20:35], v[208:211], v[196:199], v[20:35]
	ds_read_b64_tr_b16 v[208:209], v239 offset:43840
	ds_read_b64_tr_b16 v[210:211], v239 offset:44992
	ds_read_b64_tr_b16 v[40:41], v239 offset:46080
	ds_read_b64_tr_b16 v[42:43], v239 offset:47232
	s_waitcnt lgkmcnt(2)
	v_mfma_f32_32x32x16_bf16 v[4:19], v[208:211], v[196:199], v[4:19]
	s_waitcnt lgkmcnt(0)
	v_mfma_f32_32x32x16_bf16 v[20:35], v[40:43], v[36:39], v[20:35]
	ds_read_b64_tr_b16 v[40:41], v239 offset:46144
	ds_read_b64_tr_b16 v[42:43], v239 offset:47296
	s_waitcnt lgkmcnt(0)
	v_mfma_f32_32x32x16_bf16 v[4:19], v[40:43], v[36:39], v[4:19]
	ds_read_b64_tr_b16 v[40:41], v239 offset:48384
	ds_read_b64_tr_b16 v[42:43], v239 offset:49536
	v_cvt_pk_bf16_f32 v36, v78, v79
	v_cvt_pk_bf16_f32 v37, v80, v81
	v_cvt_pk_bf16_f32 v38, v82, v83
	v_cvt_pk_bf16_f32 v39, v93, v195
	s_waitcnt lgkmcnt(0)
	s_nop 0
	v_mfma_f32_32x32x16_bf16 v[20:35], v[40:43], v[36:39], v[20:35]
	ds_read_b64_tr_b16 v[40:41], v239 offset:48448
	ds_read_b64_tr_b16 v[42:43], v239 offset:49600
	s_waitcnt lgkmcnt(0)
	v_mfma_f32_32x32x16_bf16 v[4:19], v[40:43], v[36:39], v[4:19]
	ds_read_b64_tr_b16 v[40:41], v239 offset:50688
	ds_read_b64_tr_b16 v[42:43], v239 offset:51840
	v_cvt_pk_bf16_f32 v36, v70, v71
	v_cvt_pk_bf16_f32 v37, v72, v73
	v_cvt_pk_bf16_f32 v38, v74, v75
	v_cvt_pk_bf16_f32 v39, v76, v77
	s_waitcnt lgkmcnt(0)
	s_nop 0
	v_mfma_f32_32x32x16_bf16 v[20:35], v[40:43], v[36:39], v[20:35]
	ds_read_b64_tr_b16 v[40:41], v239 offset:50752
	ds_read_b64_tr_b16 v[42:43], v239 offset:51904
	s_waitcnt lgkmcnt(0)
	v_mfma_f32_32x32x16_bf16 v[4:19], v[40:43], v[36:39], v[4:19]
	ds_read_b64_tr_b16 v[40:41], v239 offset:52992
	ds_read_b64_tr_b16 v[42:43], v239 offset:54144
	v_cvt_pk_bf16_f32 v36, v62, v63
	v_cvt_pk_bf16_f32 v37, v64, v65
	v_cvt_pk_bf16_f32 v38, v66, v67
	v_cvt_pk_bf16_f32 v39, v68, v69
	s_waitcnt lgkmcnt(0)
	s_nop 0
	v_mfma_f32_32x32x16_bf16 v[20:35], v[40:43], v[36:39], v[20:35]
	ds_read_b64_tr_b16 v[40:41], v239 offset:53056
	ds_read_b64_tr_b16 v[42:43], v239 offset:54208
	s_waitcnt lgkmcnt(0)
	v_mfma_f32_32x32x16_bf16 v[4:19], v[40:43], v[36:39], v[4:19]
	ds_read_b64_tr_b16 v[40:41], v239 offset:55296
	ds_read_b64_tr_b16 v[42:43], v239 offset:56448
	v_cvt_pk_bf16_f32 v36, v54, v55
	v_cvt_pk_bf16_f32 v37, v56, v57
	v_cvt_pk_bf16_f32 v38, v58, v59
	v_cvt_pk_bf16_f32 v39, v60, v61
	s_waitcnt lgkmcnt(0)
	s_nop 0
	v_mfma_f32_32x32x16_bf16 v[20:35], v[40:43], v[36:39], v[20:35]
	ds_read_b64_tr_b16 v[40:41], v239 offset:55360
	ds_read_b64_tr_b16 v[42:43], v239 offset:56512
	s_waitcnt lgkmcnt(0)
	v_mfma_f32_32x32x16_bf16 v[4:19], v[40:43], v[36:39], v[4:19]
	ds_read_b64_tr_b16 v[40:41], v239 offset:57600
	ds_read_b64_tr_b16 v[42:43], v239 offset:58752
	v_cvt_pk_bf16_f32 v36, v46, v47
	v_cvt_pk_bf16_f32 v37, v48, v49
	v_cvt_pk_bf16_f32 v38, v50, v51
	v_cvt_pk_bf16_f32 v39, v52, v53
	s_waitcnt lgkmcnt(0)
	s_nop 0
	v_mfma_f32_32x32x16_bf16 v[20:35], v[40:43], v[36:39], v[20:35]
	ds_read_b64_tr_b16 v[40:41], v239 offset:57664
	ds_read_b64_tr_b16 v[42:43], v239 offset:58816
	s_waitcnt lgkmcnt(0)
	v_mfma_f32_32x32x16_bf16 v[4:19], v[40:43], v[36:39], v[4:19]
	v_add_f32_e32 v36, v44, v45
	v_div_scale_f32 v37, vcc, v36, v36, 1.0
	v_rcp_f32_e32 v38, v37
	s_nop 0
	v_fma_f32 v39, -v37, v38, 1.0
	v_fmac_f32_e32 v38, v39, v38
	v_div_scale_f32 v39, vcc, 1.0, v36, 1.0
	v_mul_f32_e32 v40, v39, v38
	v_fma_f32 v41, -v37, v40, v39
	v_fmac_f32_e32 v40, v41, v38
	v_fma_f32 v37, -v37, v40, v39
	v_div_fmas_f32 v37, v37, v38, v40
	v_div_fixup_f32 v36, v37, v36, 1.0
	v_pk_mul_f32 v[20:21], v[20:21], v[36:37] op_sel_hi:[1,0]
	v_pk_mul_f32 v[22:23], v[22:23], v[36:37] op_sel_hi:[1,0]
	v_pk_mul_f32 v[4:5], v[4:5], v[36:37] op_sel_hi:[1,0]
	v_pk_mul_f32 v[6:7], v[6:7], v[36:37] op_sel_hi:[1,0]
	v_lshl_add_u64 v[38:39], v[96:97], 0, v[178:179]
	v_cvt_pk_bf16_f32 v20, v20, v21
	v_cvt_pk_bf16_f32 v21, v22, v23
	v_cvt_pk_bf16_f32 v4, v4, v5
	v_cvt_pk_bf16_f32 v5, v6, v7
	global_store_dwordx2 v[38:39], v[20:21], off
	v_pk_mul_f32 v[20:21], v[24:25], v[36:37] op_sel_hi:[1,0]
	v_pk_mul_f32 v[22:23], v[26:27], v[36:37] op_sel_hi:[1,0]
	global_store_dwordx2 v[38:39], v[4:5], off offset:64
	v_pk_mul_f32 v[4:5], v[8:9], v[36:37] op_sel_hi:[1,0]
	v_pk_mul_f32 v[6:7], v[10:11], v[36:37] op_sel_hi:[1,0]
	v_cvt_pk_bf16_f32 v20, v20, v21
	v_cvt_pk_bf16_f32 v21, v22, v23
	v_cvt_pk_bf16_f32 v4, v4, v5
	v_cvt_pk_bf16_f32 v5, v6, v7
	global_store_dwordx2 v[38:39], v[20:21], off offset:16
	v_pk_mul_f32 v[20:21], v[28:29], v[36:37] op_sel_hi:[1,0]
	v_pk_mul_f32 v[22:23], v[30:31], v[36:37] op_sel_hi:[1,0]
	global_store_dwordx2 v[38:39], v[4:5], off offset:80
	v_pk_mul_f32 v[4:5], v[12:13], v[36:37] op_sel_hi:[1,0]
	v_pk_mul_f32 v[6:7], v[14:15], v[36:37] op_sel_hi:[1,0]
	v_cvt_pk_bf16_f32 v20, v20, v21
	v_cvt_pk_bf16_f32 v21, v22, v23
	v_cvt_pk_bf16_f32 v4, v4, v5
	v_cvt_pk_bf16_f32 v5, v6, v7
	global_store_dwordx2 v[38:39], v[20:21], off offset:32
	v_pk_mul_f32 v[20:21], v[32:33], v[36:37] op_sel_hi:[1,0]
	v_pk_mul_f32 v[22:23], v[34:35], v[36:37] op_sel_hi:[1,0]
	global_store_dwordx2 v[38:39], v[4:5], off offset:96
	v_pk_mul_f32 v[4:5], v[16:17], v[36:37] op_sel_hi:[1,0]
	v_pk_mul_f32 v[6:7], v[18:19], v[36:37] op_sel_hi:[1,0]
	v_cvt_pk_bf16_f32 v20, v20, v21
	v_cvt_pk_bf16_f32 v21, v22, v23
	v_cvt_pk_bf16_f32 v4, v4, v5
	v_cvt_pk_bf16_f32 v5, v6, v7
	global_store_dwordx2 v[38:39], v[20:21], off offset:48
	global_store_dwordx2 v[38:39], v[4:5], off offset:112
	s_cbranch_scc0 .LBB0_224
	v_readlane_b32 s2, v254, 39
	s_waitcnt lgkmcnt(0)
	s_barrier
	v_readlane_b32 s88, v250, 3
	s_add_i32 s43, s43, s20
	s_add_i32 s42, s42, s2
	s_add_i32 s47, s47, s20
	v_readlane_b32 s89, v250, 4
	s_cmpk_gt_i32 s43, 0xff
	s_mov_b32 s96, s88
	v_readlane_b32 s88, v254, 63
	v_readlane_b32 s90, v250, 7
	v_readlane_b32 s89, v250, 0
	s_cbranch_scc0 .LBB0_208

.LBB0_292:
	s_ashr_i32 s9, s8, 31
	s_lshl_b64 s[10:11], s[8:9], 20
	s_add_u32 s10, s33, s10
	s_addc_u32 s11, s34, s11
	s_and_b64 s[38:39], s[2:3], exec
	s_cselect_b32 s9, s11, s15
	s_cselect_b32 s13, s10, s14
	s_add_i32 s38, s57, 0x80
	v_add_u32_e32 v4, s57, v1
	s_add_u32 s59, s14, 0x10000
	v_add_u32_e32 v5, s38, v1
	v_add_u32_e32 v6, s57, v240
	v_add_u32_e32 v7, s38, v240
	v_lshl_add_u32 v245, v4, 12, v239
	s_addc_u32 s60, s15, 0
	v_mov_b32_e32 v4, 0
	v_readlane_b32 s14, v253, 24
	v_lshl_add_u32 v220, v5, 12, v239
	v_lshl_add_u32 v246, v6, 12, v241
	v_lshl_add_u32 v222, v7, 12, v241
	v_mov_b32_e32 v221, v3
	v_mov_b32_e32 v223, v3
	s_mov_b32 s61, -2
	v_readlane_b32 s15, v253, 25
	v_mov_b64_e32 v[4:5], 0
	v_mov_b64_e32 v[6:7], 0
	v_mov_b64_e32 v[8:9], 0
	v_mov_b64_e32 v[10:11], 0
	v_mov_b64_e32 v[12:13], 0
	v_mov_b64_e32 v[14:15], 0
	v_mov_b64_e32 v[16:17], 0
	v_mov_b64_e32 v[18:19], 0
	v_mov_b64_e32 v[20:21], 0
	v_mov_b64_e32 v[22:23], 0
	v_mov_b64_e32 v[24:25], 0
	v_mov_b64_e32 v[26:27], 0
	v_mov_b64_e32 v[28:29], 0
	v_mov_b64_e32 v[30:31], 0
	v_mov_b64_e32 v[32:33], 0
	v_mov_b64_e32 v[34:35], 0
	v_mov_b64_e32 v[36:37], 0
	v_mov_b64_e32 v[38:39], 0
	v_mov_b64_e32 v[40:41], 0
	v_mov_b64_e32 v[42:43], 0
	v_mov_b64_e32 v[44:45], 0
	v_mov_b64_e32 v[46:47], 0
	v_mov_b64_e32 v[48:49], 0
	v_mov_b64_e32 v[50:51], 0
	v_mov_b64_e32 v[52:53], 0
	v_mov_b64_e32 v[54:55], 0
	v_mov_b64_e32 v[56:57], 0
	v_mov_b64_e32 v[58:59], 0
	v_mov_b64_e32 v[60:61], 0
	v_mov_b64_e32 v[62:63], 0
	v_mov_b64_e32 v[64:65], 0
	v_mov_b64_e32 v[66:67], 0
	v_mov_b64_e32 v[68:69], 0
	v_mov_b64_e32 v[70:71], 0
	v_mov_b64_e32 v[72:73], 0
	v_mov_b64_e32 v[74:75], 0
	v_mov_b64_e32 v[76:77], 0
	v_mov_b64_e32 v[78:79], 0
	v_mov_b64_e32 v[80:81], 0
	v_mov_b64_e32 v[82:83], 0
	v_mov_b64_e32 v[88:89], 0
	v_mov_b64_e32 v[90:91], 0
	v_mov_b64_e32 v[92:93], 0
	v_mov_b64_e32 v[94:95], 0
	v_mov_b64_e32 v[96:97], 0
	v_mov_b64_e32 v[98:99], 0
	v_mov_b64_e32 v[100:101], 0
	v_mov_b64_e32 v[102:103], 0
	v_mov_b64_e32 v[104:105], 0
	v_mov_b64_e32 v[106:107], 0
	v_mov_b64_e32 v[108:109], 0
	v_mov_b64_e32 v[110:111], 0
	v_mov_b64_e32 v[112:113], 0
	v_mov_b64_e32 v[114:115], 0
	v_mov_b64_e32 v[116:117], 0
	v_mov_b64_e32 v[118:119], 0
	v_mov_b64_e32 v[120:121], 0
	v_mov_b64_e32 v[122:123], 0
	v_mov_b64_e32 v[124:125], 0
	v_mov_b64_e32 v[126:127], 0
	v_mov_b64_e32 v[128:129], 0
	v_mov_b64_e32 v[130:131], 0
	v_mov_b64_e32 v[132:133], 0
	v_mov_b64_e32 v[134:135], 0
	s_branch .LBB0_295

.LBB0_496:
	s_ashr_i32 s9, s8, 31
	s_lshl_b64 s[10:11], s[8:9], 20
	s_add_u32 s10, s33, s10
	s_addc_u32 s11, s34, s11
	s_and_b64 s[14:15], s[2:3], exec
	s_cselect_b32 s9, s11, s13
	s_cselect_b32 s60, s10, s12
	s_add_i32 s14, s57, 0x80
	v_add_u32_e32 v4, s57, v1
	s_add_u32 s61, s12, 0x10000
	v_add_u32_e32 v5, s14, v1
	v_add_u32_e32 v6, s57, v227
	v_add_u32_e32 v7, s14, v227
	v_lshl_add_u32 v244, v4, 12, v226
	s_addc_u32 s62, s13, 0
	v_mov_b32_e32 v4, 0
	v_readlane_b32 s12, v251, 57
	v_lshl_add_u32 v218, v5, 12, v226
	v_lshl_add_u32 v245, v6, 12, v239
	v_lshl_add_u32 v220, v7, 12, v239
	v_mov_b32_e32 v219, v3
	v_mov_b32_e32 v221, v3
	s_mov_b32 s63, -2
	v_readlane_b32 s13, v251, 58
	v_mov_b64_e32 v[4:5], 0
	v_mov_b64_e32 v[6:7], 0
	v_mov_b64_e32 v[8:9], 0
	v_mov_b64_e32 v[10:11], 0
	v_mov_b64_e32 v[12:13], 0
	v_mov_b64_e32 v[14:15], 0
	v_mov_b64_e32 v[16:17], 0
	v_mov_b64_e32 v[18:19], 0
	v_mov_b64_e32 v[20:21], 0
	v_mov_b64_e32 v[22:23], 0
	v_mov_b64_e32 v[24:25], 0
	v_mov_b64_e32 v[26:27], 0
	v_mov_b64_e32 v[28:29], 0
	v_mov_b64_e32 v[30:31], 0
	v_mov_b64_e32 v[32:33], 0
	v_mov_b64_e32 v[34:35], 0
	v_mov_b64_e32 v[36:37], 0
	v_mov_b64_e32 v[38:39], 0
	v_mov_b64_e32 v[40:41], 0
	v_mov_b64_e32 v[42:43], 0
	v_mov_b64_e32 v[44:45], 0
	v_mov_b64_e32 v[46:47], 0
	v_mov_b64_e32 v[48:49], 0
	v_mov_b64_e32 v[50:51], 0
	v_mov_b64_e32 v[52:53], 0
	v_mov_b64_e32 v[54:55], 0
	v_mov_b64_e32 v[56:57], 0
	v_mov_b64_e32 v[58:59], 0
	v_mov_b64_e32 v[60:61], 0
	v_mov_b64_e32 v[62:63], 0
	v_mov_b64_e32 v[64:65], 0
	v_mov_b64_e32 v[66:67], 0
	v_mov_b64_e32 v[68:69], 0
	v_mov_b64_e32 v[70:71], 0
	v_mov_b64_e32 v[72:73], 0
	v_mov_b64_e32 v[74:75], 0
	v_mov_b64_e32 v[76:77], 0
	v_mov_b64_e32 v[78:79], 0
	v_mov_b64_e32 v[80:81], 0
	v_mov_b64_e32 v[82:83], 0
	v_mov_b64_e32 v[88:89], 0
	v_mov_b64_e32 v[90:91], 0
	v_mov_b64_e32 v[92:93], 0
	v_mov_b64_e32 v[94:95], 0
	v_mov_b64_e32 v[96:97], 0
	v_mov_b64_e32 v[98:99], 0
	v_mov_b64_e32 v[100:101], 0
	v_mov_b64_e32 v[102:103], 0
	v_mov_b64_e32 v[104:105], 0
	v_mov_b64_e32 v[106:107], 0
	v_mov_b64_e32 v[108:109], 0
	v_mov_b64_e32 v[110:111], 0
	v_mov_b64_e32 v[112:113], 0
	v_mov_b64_e32 v[114:115], 0
	v_mov_b64_e32 v[116:117], 0
	v_mov_b64_e32 v[118:119], 0
	v_mov_b64_e32 v[120:121], 0
	v_mov_b64_e32 v[122:123], 0
	v_mov_b64_e32 v[124:125], 0
	v_mov_b64_e32 v[126:127], 0
	v_mov_b64_e32 v[128:129], 0
	v_mov_b64_e32 v[130:131], 0
	v_mov_b64_e32 v[132:133], 0
	v_mov_b64_e32 v[134:135], 0
	s_branch .LBB0_499

	.amdhsa_kernel _Z8mega_fwd8MegaArgs
		.amdhsa_group_segment_fixed_size 0
		.amdhsa_private_segment_fixed_size 0
		.amdhsa_kernarg_size 432
		.amdhsa_user_sgpr_count 2
		.amdhsa_user_sgpr_dispatch_ptr 0
		.amdhsa_user_sgpr_queue_ptr 0
		.amdhsa_user_sgpr_kernarg_segment_ptr 1
		.amdhsa_user_sgpr_dispatch_id 0
		.amdhsa_user_sgpr_kernarg_preload_length 0
		.amdhsa_user_sgpr_kernarg_preload_offset 0
		.amdhsa_user_sgpr_private_segment_size 0
		.amdhsa_uses_dynamic_stack 0
		.amdhsa_enable_private_segment 0
		.amdhsa_system_sgpr_workgroup_id_x 1
		.amdhsa_system_sgpr_workgroup_id_y 0
		.amdhsa_system_sgpr_workgroup_id_z 0
		.amdhsa_system_sgpr_workgroup_info 0
		.amdhsa_system_vgpr_workitem_id 0
		.amdhsa_next_free_vgpr 256
		.amdhsa_next_free_sgpr 102
		.amdhsa_accum_offset 256
		.amdhsa_reserve_vcc 1
		.amdhsa_float_round_mode_32 0
		.amdhsa_float_round_mode_16_64 0
		.amdhsa_float_denorm_mode_32 3
		.amdhsa_float_denorm_mode_16_64 3
		.amdhsa_dx10_clamp 1
		.amdhsa_ieee_mode 1
		.amdhsa_fp16_overflow 0
		.amdhsa_tg_split 0
		.amdhsa_exception_fp_ieee_invalid_op 0
		.amdhsa_exception_fp_denorm_src 0
		.amdhsa_exception_fp_ieee_div_zero 0
		.amdhsa_exception_fp_ieee_overflow 0
		.amdhsa_exception_fp_ieee_underflow 0
		.amdhsa_exception_fp_ieee_inexact 0
		.amdhsa_exception_int_div_zero 0
	.end_amdhsa_kernel

amdhsa.kernels:
  - .agpr_count:     0
    .args:
      - .offset:         0
        .size:           176
        .value_kind:     by_value
      - .offset:         176
        .size:           4
        .value_kind:     hidden_block_count_x
      - .offset:         180
        .size:           4
        .value_kind:     hidden_block_count_y
      - .offset:         184
        .size:           4
        .value_kind:     hidden_block_count_z
      - .offset:         188
        .size:           2
        .value_kind:     hidden_group_size_x
      - .offset:         190
        .size:           2
        .value_kind:     hidden_group_size_y
      - .offset:         192
        .size:           2
        .value_kind:     hidden_group_size_z
      - .offset:         194
        .size:           2
        .value_kind:     hidden_remainder_x
      - .offset:         196
        .size:           2
        .value_kind:     hidden_remainder_y
      - .offset:         198
        .size:           2
        .value_kind:     hidden_remainder_z
      - .offset:         216
        .size:           8
        .value_kind:     hidden_global_offset_x
      - .offset:         224
        .size:           8
        .value_kind:     hidden_global_offset_y
      - .offset:         232
        .size:           8
        .value_kind:     hidden_global_offset_z
      - .offset:         240
        .size:           2
        .value_kind:     hidden_grid_dims
      - .offset:         296
        .size:           4
        .value_kind:     hidden_dynamic_lds_size
    .group_segment_fixed_size: 0
    .kernarg_segment_align: 8
    .kernarg_segment_size: 432
    .language:       OpenCL C
    .language_version:
      - 2
      - 0
    .max_flat_workgroup_size: 512
    .name:           _Z8mega_fwd8MegaArgs
    .private_segment_fixed_size: 0
    .sgpr_count:     108
    .sgpr_spill_count: 289
    .symbol:         _Z8mega_fwd8MegaArgs.kd
    .uniform_work_group_size: 1
    .uses_dynamic_stack: false
    .vgpr_count:     256
    .vgpr_spill_count: 0
    .wavefront_size: 64
